# NSA importance-sum LDS reads batched; DSA gathered-attention masks via one unsigned compare, table-index selects dropped, first element of second half folded into batched lookups
# baseline (speedup 1.0000x reference)
.LBB0_621:
	s_waitcnt lgkmcnt(0)
	s_xor_b64 s[0:1], s[14:15], -1
	s_waitcnt vmcnt(0)
	v_mov_b32_e32 v18, 0x461c4000
	v_mov_b32_e32 v19, 0x461c4000
	v_mov_b32_e32 v20, 0x461c4000
	v_mov_b32_e32 v21, 0x461c4000
	s_and_saveexec_b64 s[14:15], s[12:13]
	s_cbranch_execz .LBB0_629
	v_add_u32_e32 v22, 0x127c, v198
	v_add_u32_e32 v23, 0x167c, v198
	v_add_u32_e32 v24, 0x1a7c, v198
	v_add_u32_e32 v25, 0x1e7c, v198
	ds_read2_b32 v[26:27], v22 offset1:1
	ds_read2_b32 v[28:29], v22 offset0:2 offset1:3
	ds_read_b32 v30, v22 offset:16
	ds_read2_b32 v[32:33], v23 offset1:1
	ds_read2_b32 v[34:35], v23 offset0:2 offset1:3
	ds_read_b32 v31, v23 offset:16
	ds_read2_b32 v[36:37], v24 offset1:1
	ds_read2_b32 v[38:39], v24 offset0:2 offset1:3
	ds_read_b32 v40, v24 offset:16
	ds_read2_b32 v[42:43], v25 offset1:1
	ds_read2_b32 v[44:45], v25 offset0:2 offset1:3
	ds_read_b32 v41, v25 offset:16
	s_waitcnt lgkmcnt(9)
	v_add_f32_e32 v18, v26, v27
	v_add_f32_e32 v18, v18, v28
	v_add_f32_e32 v18, v18, v29
	v_add_f32_e32 v18, v18, v30
	s_waitcnt lgkmcnt(6)
	v_add_f32_e32 v19, v32, v33
	v_add_f32_e32 v19, v19, v34
	v_add_f32_e32 v19, v19, v35
	v_add_f32_e32 v19, v19, v31
	s_waitcnt lgkmcnt(3)
	v_add_f32_e32 v20, v36, v37
	v_add_f32_e32 v20, v20, v38
	v_add_f32_e32 v20, v20, v39
	v_add_f32_e32 v20, v20, v40
	s_waitcnt lgkmcnt(0)
	v_add_f32_e32 v21, v42, v43
	v_add_f32_e32 v21, v21, v44
	v_add_f32_e32 v21, v21, v45
	v_add_f32_e32 v21, v21, v41

.LBB0_2601:
	ds_read_b128 v[88:91], v163
	ds_read_b128 v[92:95], v163 offset:64
	s_add_i32 s17, s16, 32
	s_cmp_lt_i32 s17, s18
	s_cselect_b32 s0, s17, s16
	s_lshl_b32 s0, s0, 2
	s_add_i32 s19, s92, s0
	s_waitcnt lgkmcnt(1)
	v_cmp_ge_u32_e64 s[0:1], s40, v88
	v_sub_u32_e32 v88, s40, v88
	v_min_i32_e32 v96, 0x3ff, v88
	s_waitcnt lgkmcnt(0)
	v_sub_u32_e32 v88, s40, v92
	v_cmp_ge_u32_e32 vcc, s40, v92
	v_min_i32_e32 v97, 0x3ff, v88
	v_sub_u32_e32 v88, s40, v89
	v_cmp_ge_u32_e64 s[4:5], s40, v89
	v_min_i32_e32 v98, 0x3ff, v88
	v_sub_u32_e32 v88, s40, v93
	v_cmp_ge_u32_e64 s[2:3], s40, v93
	v_min_i32_e32 v99, 0x3ff, v88
	v_sub_u32_e32 v88, s40, v90
	v_cmp_ge_u32_e64 s[8:9], s40, v90
	v_min_i32_e32 v100, 0x3ff, v88
	v_sub_u32_e32 v88, s40, v94
	v_cmp_ge_u32_e64 s[6:7], s40, v94
	v_min_i32_e32 v94, 0x3ff, v88
	v_sub_u32_e32 v88, s40, v91
	v_min_i32_e32 v101, 0x3ff, v88
	v_lshl_add_u32 v88, v180, 2, s19
	ds_read2_b32 v[88:89], v88 offset1:16
	v_lshl_add_u32 v102, v181, 2, s19
	ds_read2_b32 v[92:93], v102 offset1:8
	v_cmp_ge_u32_e64 s[12:13], s40, v91
	v_sub_u32_e32 v90, s40, v95
	s_waitcnt lgkmcnt(1)
	v_max_i32_e32 v198, 0, v88
	v_cmp_ge_u32_e64 s[10:11], s40, v95
	v_min_i32_e32 v95, 0x3ff, v90
	v_lshlrev_b64 v[90:91], 7, v[198:199]
	v_max_i32_e32 v198, 0, v89
	v_lshlrev_b64 v[88:89], 7, v[198:199]
	v_lshl_add_u64 v[90:91], v[178:179], 0, v[90:91]
	v_lshl_add_u64 v[88:89], v[178:179], 0, v[88:89]
	s_waitcnt lgkmcnt(0)
	v_max_i32_e32 v198, 0, v92
	global_load_dwordx4 v[148:151], v[90:91], off
	global_load_dwordx4 v[144:147], v[90:91], off offset:64
	global_load_dwordx4 v[136:139], v[88:89], off
	global_load_dwordx4 v[140:143], v[88:89], off offset:64
	v_lshlrev_b64 v[88:89], 7, v[198:199]
	v_max_i32_e32 v198, 0, v93
	ds_read2_b32 v[92:93], v102 offset0:16 offset1:24
	s_waitcnt vmcnt(4)
	v_mfma_f32_16x16x32_bf16 v[76:79], v[76:79], v[48:51], 0
	v_lshl_add_u64 v[88:89], v[176:177], 0, v[88:89]
	v_lshlrev_b64 v[90:91], 7, v[198:199]
	v_lshl_add_u64 v[90:91], v[176:177], 0, v[90:91]
	s_waitcnt lgkmcnt(0)
	v_max_i32_e32 v198, 0, v92
	global_load_dwordx4 v[104:107], v[88:89], off
	global_load_dwordx4 v[108:111], v[90:91], off
	v_lshlrev_b64 v[88:89], 7, v[198:199]
	v_max_i32_e32 v198, 0, v93
	v_mfma_f32_16x16x32_bf16 v[72:75], v[72:75], v[52:55], v[76:79]
	s_add_i32 s20, 0, 0x22200
	s_cmp_ge_i32 s17, s18
	v_lshl_add_u64 v[76:77], v[176:177], 0, v[88:89]
	v_lshlrev_b64 v[78:79], 7, v[198:199]
	v_lshl_add_u64 v[78:79], v[176:177], 0, v[78:79]
	global_load_dwordx4 v[112:115], v[76:77], off
	global_load_dwordx4 v[116:119], v[78:79], off
	v_mfma_f32_16x16x32_bf16 v[60:63], v[60:63], v[48:51], 0
	v_add_u32_e32 v76, s20, v100
	v_add_u32_e32 v77, s20, v94
	v_add_u32_e32 v78, s20, v101
	v_mfma_f32_16x16x32_bf16 v[56:59], v[56:59], v[52:55], v[60:63]
	v_add_u32_e32 v79, s20, v95
	s_nop 2
	v_add_u32_e32 v60, s20, v96
	v_add_u32_e32 v61, s20, v97
	v_add_u32_e32 v62, s20, v98
	v_add_u32_e32 v63, s20, v99
	ds_read_u8 v60, v60
	ds_read_u8 v61, v61
	ds_read_u8 v62, v62
	ds_read_u8 v63, v63
	ds_read_u8 v76, v76
	ds_read_u8 v77, v77
	ds_read_u8 v78, v78
	ds_read_u8 v79, v79
	s_waitcnt lgkmcnt(7)
	v_lshl_add_u32 v60, v60, 6, v249
	s_waitcnt lgkmcnt(6)
	v_lshl_add_u32 v61, v61, 6, v249
	s_waitcnt lgkmcnt(5)
	v_lshl_add_u32 v62, v62, 6, v249
	s_waitcnt lgkmcnt(4)
	v_lshl_add_u32 v63, v63, 6, v249
	s_waitcnt lgkmcnt(3)
	v_lshl_add_u32 v76, v76, 6, v249
	s_waitcnt lgkmcnt(2)
	v_lshl_add_u32 v77, v77, 6, v249
	s_waitcnt lgkmcnt(1)
	v_lshl_add_u32 v78, v78, 6, v249
	s_waitcnt lgkmcnt(0)
	v_lshl_add_u32 v79, v79, 6, v249
	ds_read_b32 v60, v60
	ds_read_b32 v61, v61
	ds_read_b32 v62, v62
	ds_read_b32 v63, v63
	ds_read_b32 v76, v76
	ds_read_b32 v77, v77
	ds_read_b32 v78, v78
	ds_read_b32 v79, v79
	s_waitcnt lgkmcnt(7)
	v_add_f32_e32 v60, v72, v60
	s_waitcnt lgkmcnt(6)
	v_add_f32_e32 v56, v56, v61
	s_waitcnt lgkmcnt(5)
	v_add_f32_e32 v61, v73, v62
	s_waitcnt lgkmcnt(4)
	v_add_f32_e32 v57, v57, v63
	s_waitcnt lgkmcnt(3)
	v_add_f32_e32 v62, v74, v76
	s_waitcnt lgkmcnt(2)
	v_add_f32_e32 v58, v58, v77
	s_waitcnt lgkmcnt(1)
	v_add_f32_e32 v63, v75, v78
	s_waitcnt lgkmcnt(0)
	v_add_f32_e32 v59, v59, v79
	v_exp_f32_e32 v60, v60
	v_exp_f32_e32 v61, v61
	v_exp_f32_e32 v62, v62
	v_exp_f32_e32 v63, v63
	v_exp_f32_e32 v56, v56
	v_exp_f32_e32 v57, v57
	v_exp_f32_e32 v58, v58
	v_exp_f32_e32 v59, v59
	ds_write_b128 v243, v[64:67]
	ds_write_b128 v243, v[68:71] offset:1152
	ds_write_b128 v243, v[80:83] offset:2304
	ds_write_b128 v243, v[84:87] offset:3456
	v_cndmask_b32_e64 v76, 0, v60, s[0:1]
	v_cndmask_b32_e64 v77, 0, v61, s[4:5]
	v_cndmask_b32_e64 v78, 0, v62, s[8:9]
	v_cndmask_b32_e64 v79, 0, v63, s[12:13]
	v_cndmask_b32_e32 v96, 0, v56, vcc
	v_cndmask_b32_e64 v97, 0, v57, s[2:3]
	v_cndmask_b32_e64 v98, 0, v58, s[6:7]
	v_cndmask_b32_e64 v99, 0, v59, s[10:11]
	v_cvt_pk_bf16_f32 v56, v76, v77
	v_cvt_pk_bf16_f32 v57, v78, v79
	v_cvt_pk_bf16_f32 v58, v96, v97
	v_cvt_pk_bf16_f32 v59, v98, v99
	ds_read_b64_tr_b16 v[62:63], v244 offset:2304
	ds_read_b64_tr_b16 v[60:61], v244
	ds_read_b64_tr_b16 v[64:65], v244 offset:32
	ds_read_b64_tr_b16 v[68:69], v244 offset:64
	ds_read_b64_tr_b16 v[72:73], v244 offset:96
	ds_read_b64_tr_b16 v[66:67], v244 offset:2336
	ds_read_b64_tr_b16 v[70:71], v244 offset:2368
	ds_read_b64_tr_b16 v[74:75], v244 offset:2400
	s_waitcnt lgkmcnt(6)
	v_mfma_f32_16x16x32_bf16 v[88:91], v[56:59], v[60:63], v[132:135]
	v_add_f32_e32 v60, 0, v76
	v_add_f32_e32 v60, v60, v77
	v_add_f32_e32 v60, v60, v78
	v_add_f32_e32 v60, v60, v79
	v_add_f32_e32 v60, v96, v60
	v_add_f32_e32 v60, v97, v60
	v_add_f32_e32 v60, v98, v60
	s_waitcnt lgkmcnt(2)
	v_mfma_f32_16x16x32_bf16 v[92:95], v[56:59], v[64:67], v[128:131]
	v_add_f32_e32 v60, v99, v60
	v_add_f32_e32 v165, v167, v60
	s_waitcnt lgkmcnt(1)
	v_mfma_f32_16x16x32_bf16 v[100:103], v[56:59], v[68:71], v[124:127]
	s_mov_b64 s[0:1], -1
	s_mov_b64 s[14:15], -1
	s_waitcnt lgkmcnt(0)
	v_mfma_f32_16x16x32_bf16 v[96:99], v[56:59], v[72:75], v[120:123]
	s_cbranch_scc1 .LBB0_2605
	s_add_i32 s19, s16, 64
	s_cmp_ge_i32 s19, s18
	s_cselect_b64 s[14:15], -1, 0
	s_cmp_lt_i32 s19, s18
	s_cselect_b32 s0, s19, s16
	s_lshl_b32 s0, s0, 2
	s_add_i32 s0, s92, s0
	v_lshl_add_u32 v56, v180, 2, s0
	ds_read2_b32 v[56:57], v56 offset1:16
	v_lshl_add_u32 v80, v181, 2, s0
	s_waitcnt vmcnt(7)
	v_mfma_f32_16x16x32_bf16 v[120:123], v[148:151], v[48:51], 0
	s_waitcnt lgkmcnt(0)
	v_max_i32_e32 v198, 0, v56
	v_lshlrev_b64 v[58:59], 7, v[198:199]
	v_max_i32_e32 v198, 0, v57
	v_lshlrev_b64 v[56:57], 7, v[198:199]
	v_lshl_add_u64 v[58:59], v[178:179], 0, v[58:59]
	v_lshl_add_u64 v[56:57], v[178:179], 0, v[56:57]
	global_load_dwordx4 v[76:79], v[58:59], off
	global_load_dwordx4 v[72:75], v[58:59], off offset:64
	global_load_dwordx4 v[60:63], v[56:57], off
	s_nop 0
	global_load_dwordx4 v[56:59], v[56:57], off offset:64
	ds_read2_b32 v[68:69], v80 offset1:8
	ds_read2_b32 v[84:85], v80 offset0:16 offset1:24
	ds_read_b128 v[128:131], v163 offset:128
	ds_read_b128 v[132:135], v163 offset:192
	s_waitcnt vmcnt(10)
	v_mfma_f32_16x16x32_bf16 v[124:127], v[144:147], v[52:55], v[120:123]
	s_waitcnt lgkmcnt(3)
	v_max_i32_e32 v198, 0, v68
	v_lshlrev_b64 v[64:65], 7, v[198:199]
	v_max_i32_e32 v198, 0, v69
	v_lshlrev_b64 v[68:69], 7, v[198:199]
	s_waitcnt lgkmcnt(2)
	v_max_i32_e32 v198, 0, v84
	v_lshlrev_b64 v[80:81], 7, v[198:199]
	v_max_i32_e32 v198, 0, v85
	v_lshlrev_b64 v[84:85], 7, v[198:199]
	v_lshl_add_u64 v[64:65], v[176:177], 0, v[64:65]
	v_lshl_add_u64 v[68:69], v[176:177], 0, v[68:69]
	v_lshl_add_u64 v[80:81], v[176:177], 0, v[80:81]
	v_lshl_add_u64 v[84:85], v[176:177], 0, v[84:85]
	global_load_dwordx4 v[64:67], v[64:65], off
	s_waitcnt lgkmcnt(1)
	v_cmp_ge_u32_e64 s[16:17], s40, v128
	global_load_dwordx4 v[68:71], v[68:69], off
	global_load_dwordx4 v[80:83], v[80:81], off
	global_load_dwordx4 v[84:87], v[84:85], off
	s_waitcnt lgkmcnt(0)
	v_cmp_ge_u32_e32 vcc, s40, v132
	v_cmp_ge_u32_e64 s[0:1], s40, v129
	v_cmp_ge_u32_e64 s[2:3], s40, v133
	v_cmp_ge_u32_e64 s[4:5], s40, v130
	v_cmp_ge_u32_e64 s[6:7], s40, v134
	v_cmp_ge_u32_e64 s[8:9], s40, v131
	v_sub_u32_e32 v132, s40, v132
	v_sub_u32_e32 v129, s40, v129
	v_sub_u32_e32 v133, s40, v133
	v_sub_u32_e32 v130, s40, v130
	v_sub_u32_e32 v134, s40, v134
	v_sub_u32_e32 v131, s40, v131
	v_cmp_ge_u32_e64 s[10:11], s40, v135
	v_sub_u32_e32 v135, s40, v135
	v_min_i32_e32 v132, 0x3ff, v132
	v_min_i32_e32 v129, 0x3ff, v129
	v_min_i32_e32 v133, 0x3ff, v133
	v_min_i32_e32 v130, 0x3ff, v130
	v_min_i32_e32 v134, 0x3ff, v134
	v_min_i32_e32 v131, 0x3ff, v131
	v_min_i32_e32 v135, 0x3ff, v135
	v_sub_u32_e32 v128, s40, v128
	v_min_i32_e32 v128, 0x3ff, v128
	v_add_u32_e32 v128, s20, v128
	v_add_u32_e32 v132, s20, v132
	v_add_u32_e32 v129, s20, v129
	v_add_u32_e32 v133, s20, v133
	v_add_u32_e32 v130, s20, v130
	v_add_u32_e32 v134, s20, v134
	v_add_u32_e32 v131, s20, v131
	v_add_u32_e32 v135, s20, v135
	ds_read_u8 v128, v128
	ds_read_u8 v132, v132
	ds_read_u8 v129, v129
	ds_read_u8 v133, v133
	ds_read_u8 v130, v130
	ds_read_u8 v134, v134
	ds_read_u8 v135, v135
	ds_read_u8 v131, v131
	s_waitcnt vmcnt(13)
	v_mfma_f32_16x16x32_bf16 v[120:123], v[136:139], v[48:51], 0
	s_waitcnt lgkmcnt(7)
	v_lshl_add_u32 v128, v128, 6, v249
	s_waitcnt lgkmcnt(6)
	v_lshl_add_u32 v132, v132, 6, v249
	s_waitcnt lgkmcnt(5)
	v_lshl_add_u32 v129, v129, 6, v249
	s_waitcnt lgkmcnt(4)
	v_lshl_add_u32 v133, v133, 6, v249
	s_waitcnt lgkmcnt(3)
	v_lshl_add_u32 v130, v130, 6, v249
	s_waitcnt lgkmcnt(2)
	v_lshl_add_u32 v134, v134, 6, v249
	s_waitcnt lgkmcnt(0)
	v_lshl_add_u32 v131, v131, 6, v249
	v_lshl_add_u32 v135, v135, 6, v249
	ds_read_b32 v128, v128
	ds_read_b32 v132, v132
	ds_read_b32 v129, v129
	ds_read_b32 v133, v133
	ds_read_b32 v130, v130
	ds_read_b32 v134, v134
	ds_read_b32 v135, v135
	ds_read_b32 v131, v131
	s_waitcnt vmcnt(12)
	v_mfma_f32_16x16x32_bf16 v[120:123], v[140:143], v[52:55], v[120:123]
	s_waitcnt lgkmcnt(7)
	v_add_f32_e32 v124, v124, v128
	v_exp_f32_e32 v136, v124
	s_waitcnt lgkmcnt(6)
	s_nop 3
	v_add_f32_e32 v120, v120, v132
	s_waitcnt lgkmcnt(5)
	v_add_f32_e32 v124, v125, v129
	s_waitcnt lgkmcnt(4)
	v_add_f32_e32 v121, v121, v133
	s_waitcnt lgkmcnt(3)
	v_add_f32_e32 v125, v126, v130
	s_waitcnt lgkmcnt(2)
	v_add_f32_e32 v122, v122, v134
	s_waitcnt lgkmcnt(0)
	v_add_f32_e32 v126, v127, v131
	v_add_f32_e32 v123, v123, v135
	v_exp_f32_e32 v124, v124
	v_exp_f32_e32 v125, v125
	v_exp_f32_e32 v126, v126
	v_exp_f32_e32 v120, v120
	v_exp_f32_e32 v121, v121
	v_exp_f32_e32 v122, v122
	v_exp_f32_e32 v123, v123
	s_waitcnt vmcnt(11)
	ds_write_b128 v243, v[104:107]
	s_waitcnt vmcnt(10)
	ds_write_b128 v243, v[108:111] offset:1152
	s_waitcnt vmcnt(9)
	ds_write_b128 v243, v[112:115] offset:2304
	s_waitcnt vmcnt(8)
	ds_write_b128 v243, v[116:119] offset:3456
	v_cndmask_b32_e64 v136, 0, v136, s[16:17]
	v_cndmask_b32_e64 v124, 0, v124, s[0:1]
	v_cndmask_b32_e64 v125, 0, v125, s[4:5]
	v_cndmask_b32_e64 v126, 0, v126, s[8:9]
	v_cndmask_b32_e32 v127, 0, v120, vcc
	v_cndmask_b32_e64 v137, 0, v121, s[2:3]
	v_cndmask_b32_e64 v138, 0, v122, s[6:7]
	v_cndmask_b32_e64 v139, 0, v123, s[10:11]
	v_cvt_pk_bf16_f32 v104, v136, v124
	v_cvt_pk_bf16_f32 v105, v125, v126
	v_cvt_pk_bf16_f32 v106, v127, v137
	v_cvt_pk_bf16_f32 v107, v138, v139
	ds_read_b64_tr_b16 v[110:111], v244 offset:2304
	ds_read_b64_tr_b16 v[108:109], v244
	ds_read_b64_tr_b16 v[112:113], v244 offset:32
	ds_read_b64_tr_b16 v[116:117], v244 offset:64
	ds_read_b64_tr_b16 v[120:121], v244 offset:96
	ds_read_b64_tr_b16 v[114:115], v244 offset:2336
	ds_read_b64_tr_b16 v[118:119], v244 offset:2368
	ds_read_b64_tr_b16 v[122:123], v244 offset:2400
	s_waitcnt lgkmcnt(6)
	v_mfma_f32_16x16x32_bf16 v[132:135], v[104:107], v[108:111], v[88:91]
	v_add_f32_e32 v108, 0, v136
	v_add_f32_e32 v108, v124, v108
	v_add_f32_e32 v108, v125, v108
	v_add_f32_e32 v108, v126, v108
	v_add_f32_e32 v108, v127, v108
	s_waitcnt lgkmcnt(2)
	v_mfma_f32_16x16x32_bf16 v[128:131], v[104:107], v[112:115], v[92:95]
	v_add_f32_e32 v108, v137, v108
	v_add_f32_e32 v108, v138, v108
	s_waitcnt lgkmcnt(1)
	v_mfma_f32_16x16x32_bf16 v[124:127], v[104:107], v[116:119], v[100:103]
	v_add_f32_e32 v108, v139, v108
	v_add_f32_e32 v167, v165, v108
	v_add_u32_e32 v163, 0x100, v163
	s_waitcnt lgkmcnt(0)
	v_mfma_f32_16x16x32_bf16 v[120:123], v[104:107], v[120:123], v[96:99]
	s_mov_b64 s[0:1], 0
